# v50 + P5 LayerNorm affine tail: gamma/beta quads kept two column tiles ahead in registers unused in this phase (counted waits)
# baseline (speedup 1.0000x reference)
.LBB0_768:
	s_or_b64 exec, exec, s[10:11]
	s_waitcnt lgkmcnt(1)
	v_and_b32_e32 v94, 0x78, v102
	v_add_u32_e32 v114, 0, v94
	v_add_u32_e32 v94, 0x20000, v114
	v_add_u32_e32 v96, 0x20200, v114
	s_waitcnt lgkmcnt(0)
	s_barrier
	v_add_u32_e32 v102, 0x20400, v114
	v_add_u32_e32 v110, 0x20600, v114
	ds_read_b64 v[94:95], v94
	ds_read_b64 v[96:97], v96
	ds_read_b64 v[104:105], v102
	ds_read_b64 v[112:113], v110
	v_add_u32_e32 v116, 0x20800, v114
	s_waitcnt lgkmcnt(3)
	v_pk_add_f32 v[94:95], v[94:95], 0 op_sel_hi:[1,0]
	v_add_u32_e32 v117, 0x20a00, v114
	v_add_u32_e32 v146, 0x20c00, v114
	s_waitcnt lgkmcnt(2)
	v_pk_add_f32 v[94:95], v[94:95], v[96:97]
	v_add_u32_e32 v102, 0x20e00, v114
	s_waitcnt lgkmcnt(1)
	v_pk_add_f32 v[94:95], v[94:95], v[104:105]
	ds_read_b64 v[96:97], v116
	ds_read_b64 v[104:105], v117
	ds_read_b64 v[116:117], v146
	ds_read_b64 v[146:147], v102
	s_waitcnt lgkmcnt(4)
	v_pk_add_f32 v[94:95], v[94:95], v[112:113]
	v_add_u32_e32 v112, 0x20480, v114
	s_waitcnt lgkmcnt(3)
	v_pk_add_f32 v[94:95], v[94:95], v[96:97]
	v_add_u32_e32 v148, 0x20880, v114
	s_waitcnt lgkmcnt(2)
	v_pk_add_f32 v[94:95], v[94:95], v[104:105]
	v_add_u32_e32 v149, 0x20a80, v114
	s_waitcnt lgkmcnt(1)
	v_pk_add_f32 v[94:95], v[94:95], v[116:117]
	v_add_u32_e32 v150, 0x20c80, v114
	s_waitcnt lgkmcnt(0)
	v_pk_add_f32 v[94:95], v[94:95], v[146:147]
	v_add_u32_e32 v146, 0x20680, v114
	v_pk_mul_f32 v[94:95], v[94:95], s[66:67] op_sel_hi:[1,0]
	v_add_u32_e32 v151, 0x20e80, v114
	v_fma_f32 v96, -v94, v94, v95
	v_max_f32_e32 v96, 0, v96
	v_add_f32_e32 v96, 0x3727c5ac, v96
	v_mul_f32_e32 v97, 0x4f800000, v96
	v_cmp_gt_f32_e32 vcc, s89, v96
	v_add_u32_e32 v160, 0x20780, v114
	v_add_u32_e32 v162, 0x20980, v114
	v_cndmask_b32_e32 v96, v96, v97, vcc
	v_sqrt_f32_e32 v97, v96
	v_add_u32_e32 v163, 0x20b80, v114
	v_add_u32_e32 v164, 0x20d80, v114
	v_pk_add_f32 v[82:83], v[82:83], v[94:95] op_sel_hi:[1,0] neg_lo:[0,1] neg_hi:[0,1]
	v_add_u32_e32 v102, -1, v97
	v_fma_f32 v104, -v102, v97, v96
	v_cmp_ge_f32_e64 s[10:11], 0, v104
	v_add_u32_e32 v104, 1, v97
	v_pk_add_f32 v[84:85], v[84:85], v[94:95] op_sel_hi:[1,0] neg_lo:[0,1] neg_hi:[0,1]
	v_cndmask_b32_e64 v102, v97, v102, s[10:11]
	v_fma_f32 v97, -v104, v97, v96
	v_cmp_lt_f32_e64 s[10:11], 0, v97
	v_and_b32_e32 v117, 15, v223
	v_pk_add_f32 v[70:71], v[70:71], v[94:95] op_sel_hi:[1,0] neg_lo:[0,1] neg_hi:[0,1]
	v_cndmask_b32_e64 v97, v102, v104, s[10:11]
	v_mul_f32_e32 v102, 0x37800000, v97
	v_cndmask_b32_e32 v97, v97, v102, vcc
	v_cmp_class_f32_e32 vcc, v96, v216
	v_add_u32_e32 v104, 0x20280, v114
	v_pk_add_f32 v[72:73], v[72:73], v[94:95] op_sel_hi:[1,0] neg_lo:[0,1] neg_hi:[0,1]
	v_cndmask_b32_e32 v102, v97, v96, vcc
	v_div_scale_f32 v110, s[10:11], v102, v102, 1.0
	v_rcp_f32_e32 v116, v110
	v_div_scale_f32 v152, vcc, 1.0, v102, 1.0
	v_pk_add_f32 v[62:63], v[62:63], v[94:95] op_sel_hi:[1,0] neg_lo:[0,1] neg_hi:[0,1]
	v_fma_f32 v96, -v110, v116, 1.0
	v_fmac_f32_e32 v116, v96, v116
	v_add_u32_e32 v96, 0x20080, v114
	ds_read_b64 v[96:97], v96
	ds_read_b64 v[104:105], v104
	ds_read_b64 v[112:113], v112
	ds_read_b64 v[146:147], v146
	v_mul_f32_e32 v153, v152, v116
	s_waitcnt lgkmcnt(3)
	v_pk_add_f32 v[96:97], v[96:97], 0 op_sel_hi:[1,0]
	v_pk_add_f32 v[64:65], v[64:65], v[94:95] op_sel_hi:[1,0] neg_lo:[0,1] neg_hi:[0,1]
	s_waitcnt lgkmcnt(2)
	v_pk_add_f32 v[96:97], v[96:97], v[104:105]
	v_pk_add_f32 v[58:59], v[58:59], v[94:95] op_sel_hi:[1,0] neg_lo:[0,1] neg_hi:[0,1]
	s_waitcnt lgkmcnt(1)
	v_pk_add_f32 v[96:97], v[96:97], v[112:113]
	ds_read_b64 v[104:105], v148
	ds_read_b64 v[112:113], v149
	ds_read_b64 v[148:149], v150
	ds_read_b64 v[150:151], v151
	s_waitcnt lgkmcnt(4)
	v_pk_add_f32 v[96:97], v[96:97], v[146:147]
	v_add_u32_e32 v146, 0x20500, v114
	s_waitcnt lgkmcnt(3)
	v_pk_add_f32 v[96:97], v[96:97], v[104:105]
	v_pk_add_f32 v[60:61], v[60:61], v[94:95] op_sel_hi:[1,0] neg_lo:[0,1] neg_hi:[0,1]
	s_waitcnt lgkmcnt(2)
	v_pk_add_f32 v[96:97], v[96:97], v[112:113]
	v_fma_f32 v112, -v110, v153, v152
	s_waitcnt lgkmcnt(1)
	v_pk_add_f32 v[96:97], v[96:97], v[148:149]
	v_fmac_f32_e32 v153, v112, v116
	s_waitcnt lgkmcnt(0)
	v_pk_add_f32 v[96:97], v[96:97], v[150:151]
	v_fma_f32 v110, -v110, v153, v152
	v_pk_mul_f32 v[96:97], v[96:97], s[66:67] op_sel_hi:[1,0]
	v_add_u32_e32 v148, 0x20700, v114
	v_fma_f32 v104, -v96, v96, v97
	v_max_f32_e32 v104, 0, v104
	v_add_f32_e32 v104, 0x3727c5ac, v104
	v_mul_f32_e32 v105, 0x4f800000, v104
	v_cmp_gt_f32_e64 s[10:11], s89, v104
	v_add_u32_e32 v150, 0x20900, v114
	v_add_u32_e32 v151, 0x20b00, v114
	v_cndmask_b32_e64 v104, v104, v105, s[10:11]
	v_sqrt_f32_e32 v105, v104
	v_add_u32_e32 v152, 0x20d00, v114
	v_pk_add_f32 v[54:55], v[54:55], v[94:95] op_sel_hi:[1,0] neg_lo:[0,1] neg_hi:[0,1]
	v_pk_add_f32 v[56:57], v[56:57], v[94:95] op_sel_hi:[1,0] neg_lo:[0,1] neg_hi:[0,1]
	v_add_u32_e32 v112, -1, v105
	v_fma_f32 v113, -v112, v105, v104
	v_cmp_ge_f32_e64 s[12:13], 0, v113
	v_add_u32_e32 v113, 1, v105
	v_pk_add_f32 v[38:39], v[38:39], v[94:95] op_sel_hi:[1,0] neg_lo:[0,1] neg_hi:[0,1]
	v_cndmask_b32_e64 v112, v105, v112, s[12:13]
	v_fma_f32 v105, -v113, v105, v104
	v_cmp_lt_f32_e64 s[12:13], 0, v105
	v_pk_add_f32 v[40:41], v[40:41], v[94:95] op_sel_hi:[1,0] neg_lo:[0,1] neg_hi:[0,1]
	v_pk_add_f32 v[22:23], v[22:23], v[94:95] op_sel_hi:[1,0] neg_lo:[0,1] neg_hi:[0,1]
	v_cndmask_b32_e64 v105, v112, v113, s[12:13]
	v_mul_f32_e32 v112, 0x37800000, v105
	v_cndmask_b32_e64 v105, v105, v112, s[10:11]
	v_cmp_class_f32_e64 s[10:11], v104, v216
	v_add_u32_e32 v112, 0x20300, v114
	v_pk_add_f32 v[24:25], v[24:25], v[94:95] op_sel_hi:[1,0] neg_lo:[0,1] neg_hi:[0,1]
	v_cndmask_b32_e64 v158, v105, v104, s[10:11]
	v_div_scale_f32 v154, s[10:11], v158, v158, 1.0
	v_rcp_f32_e32 v155, v154
	v_div_fmas_f32 v104, v110, v116, v153
	v_div_fixup_f32 v102, v104, v102, 1.0
	v_div_scale_f32 v110, vcc, 1.0, v158, 1.0
	v_fma_f32 v104, -v154, v155, 1.0
	v_fmac_f32_e32 v155, v104, v155
	v_mul_f32_e32 v116, v110, v155
	v_fma_f32 v104, -v154, v116, v110
	v_fmac_f32_e32 v116, v104, v155
	v_add_u32_e32 v104, 0x20100, v114
	ds_read_b64 v[104:105], v104
	ds_read_b64 v[112:113], v112
	ds_read_b64 v[146:147], v146
	ds_read_b64 v[148:149], v148
	v_add_u32_e32 v153, 0x20f00, v114
	s_waitcnt lgkmcnt(3)
	v_pk_add_f32 v[104:105], v[104:105], 0 op_sel_hi:[1,0]
	v_fma_f32 v110, -v154, v116, v110
	s_waitcnt lgkmcnt(2)
	v_pk_add_f32 v[104:105], v[104:105], v[112:113]
	v_div_fmas_f32 v110, v110, v155, v116
	s_waitcnt lgkmcnt(1)
	v_pk_add_f32 v[104:105], v[104:105], v[146:147]
	ds_read_b64 v[112:113], v150
	ds_read_b64 v[146:147], v151
	ds_read_b64 v[150:151], v152
	ds_read_b64 v[152:153], v153
	s_waitcnt lgkmcnt(4)
	v_pk_add_f32 v[104:105], v[104:105], v[148:149]
	v_div_fixup_f32 v110, v110, v158, 1.0
	s_waitcnt lgkmcnt(3)
	v_pk_add_f32 v[104:105], v[104:105], v[112:113]
	v_add_u32_e32 v158, 0x20580, v114
	s_waitcnt lgkmcnt(2)
	v_pk_add_f32 v[104:105], v[104:105], v[146:147]
	v_pk_mul_f32 v[82:83], v[82:83], v[102:103] op_sel_hi:[1,0]
	s_waitcnt lgkmcnt(1)
	v_pk_add_f32 v[104:105], v[104:105], v[150:151]
	v_pk_mul_f32 v[84:85], v[84:85], v[102:103] op_sel_hi:[1,0]
	s_waitcnt lgkmcnt(0)
	v_pk_add_f32 v[104:105], v[104:105], v[152:153]
	v_pk_mul_f32 v[70:71], v[70:71], v[102:103] op_sel_hi:[1,0]
	v_pk_mul_f32 v[104:105], v[104:105], s[66:67] op_sel_hi:[1,0]
	v_pk_mul_f32 v[72:73], v[72:73], v[102:103] op_sel_hi:[1,0]
	v_fma_f32 v112, -v104, v104, v105
	v_max_f32_e32 v112, 0, v112
	v_add_f32_e32 v112, 0x3727c5ac, v112
	v_mul_f32_e32 v113, 0x4f800000, v112
	v_cmp_gt_f32_e64 s[10:11], s89, v112
	v_pk_mul_f32 v[62:63], v[62:63], v[102:103] op_sel_hi:[1,0]
	v_pk_mul_f32 v[64:65], v[64:65], v[102:103] op_sel_hi:[1,0]
	v_cndmask_b32_e64 v112, v112, v113, s[10:11]
	v_sqrt_f32_e32 v113, v112
	v_pk_mul_f32 v[58:59], v[58:59], v[102:103] op_sel_hi:[1,0]
	v_pk_mul_f32 v[60:61], v[60:61], v[102:103] op_sel_hi:[1,0]
	v_pk_mul_f32 v[54:55], v[54:55], v[102:103] op_sel_hi:[1,0]
	v_add_u32_e32 v116, -1, v113
	v_fma_f32 v146, -v116, v113, v112
	v_cmp_ge_f32_e32 vcc, 0, v146
	v_add_u32_e32 v146, 1, v113
	v_pk_mul_f32 v[56:57], v[56:57], v[102:103] op_sel_hi:[1,0]
	v_cndmask_b32_e32 v116, v113, v116, vcc
	v_fma_f32 v113, -v146, v113, v112
	v_cmp_lt_f32_e32 vcc, 0, v113
	v_pk_add_f32 v[46:47], v[46:47], v[104:105] op_sel_hi:[1,0] neg_lo:[0,1] neg_hi:[0,1]
	v_pk_add_f32 v[48:49], v[48:49], v[104:105] op_sel_hi:[1,0] neg_lo:[0,1] neg_hi:[0,1]
	v_cndmask_b32_e32 v113, v116, v146, vcc
	v_mul_f32_e32 v116, 0x37800000, v113
	v_cndmask_b32_e64 v113, v113, v116, s[10:11]
	v_cmp_class_f32_e32 vcc, v112, v216
	v_pk_mul_f32 v[38:39], v[38:39], v[102:103] op_sel_hi:[1,0]
	v_pk_mul_f32 v[40:41], v[40:41], v[102:103] op_sel_hi:[1,0]
	v_cndmask_b32_e32 v116, v113, v112, vcc
	v_lshrrev_b32_e32 v112, 2, v223
	v_and_or_b32 v146, v112, 12, s35
	v_ashrrev_i32_e32 v147, 31, v146
	v_lshlrev_b64 v[112:113], 2, v[146:147]
	v_lshlrev_b32_e32 v238, 2, v146
	v_lshlrev_b32_e32 v242, 2, v146
	global_load_dwordx4 v[238:241], v238, s[8:9]
	global_load_dwordx4 v[242:245], v242, s[20:21]
	v_lshlrev_b32_e32 v246, 2, v146
	v_lshlrev_b32_e32 v250, 2, v146
	global_load_dwordx4 v[246:249], v246, s[8:9] offset:64
	global_load_dwordx4 v[250:253], v250, s[20:21] offset:64
	v_lshl_add_u64 v[148:149], s[8:9], 0, v[112:113]
	v_lshl_add_u64 v[112:113], s[20:21], 0, v[112:113]
	v_div_scale_f32 v166, s[10:11], v116, v116, 1.0
	v_rcp_f32_e32 v167, v166
	v_add_u32_e32 v148, 0x20380, v114
	v_div_scale_f32 v147, vcc, 1.0, v116, 1.0
	v_fma_f32 v112, -v166, v167, 1.0
	v_fmac_f32_e32 v167, v112, v167
	v_add_u32_e32 v112, 0x20180, v114
	ds_read_b64 v[112:113], v112
	ds_read_b64 v[148:149], v148
	ds_read_b64 v[158:159], v158
	ds_read_b64 v[160:161], v160
	v_add_u32_e32 v114, 0x20f80, v114
	s_waitcnt lgkmcnt(3)
	v_pk_add_f32 v[112:113], v[112:113], 0 op_sel_hi:[1,0]
	v_mul_f32_e32 v168, v147, v167
	s_waitcnt lgkmcnt(2)
	v_pk_add_f32 v[112:113], v[112:113], v[148:149]
	v_pk_add_f32 v[34:35], v[34:35], v[104:105] op_sel_hi:[1,0] neg_lo:[0,1] neg_hi:[0,1]
	s_waitcnt lgkmcnt(1)
	v_pk_add_f32 v[112:113], v[112:113], v[158:159]
	ds_read_b64 v[148:149], v162
	ds_read_b64 v[158:159], v163
	ds_read_b64 v[162:163], v164
	ds_read_b64 v[164:165], v114
	s_waitcnt lgkmcnt(4)
	v_pk_add_f32 v[112:113], v[112:113], v[160:161]
	v_pk_add_f32 v[36:37], v[36:37], v[104:105] op_sel_hi:[1,0] neg_lo:[0,1] neg_hi:[0,1]
	s_waitcnt lgkmcnt(3)
	v_pk_add_f32 v[112:113], v[112:113], v[148:149]
	v_fma_f32 v149, -v166, v168, v147
	s_waitcnt lgkmcnt(2)
	v_pk_add_f32 v[112:113], v[112:113], v[158:159]
	v_fmac_f32_e32 v168, v149, v167
	s_waitcnt lgkmcnt(1)
	v_pk_add_f32 v[112:113], v[112:113], v[162:163]
	v_fma_f32 v147, -v166, v168, v147
	s_waitcnt lgkmcnt(0)
	v_pk_add_f32 v[112:113], v[112:113], v[164:165]
	v_pk_mul_f32 v[22:23], v[22:23], v[102:103] op_sel_hi:[1,0]
	v_pk_mul_f32 v[112:113], v[112:113], s[66:67] op_sel_hi:[1,0]
	v_pk_mul_f32 v[24:25], v[24:25], v[102:103] op_sel_hi:[1,0]
	v_fma_f32 v114, -v112, v112, v113
	v_max_f32_e32 v114, 0, v114
	v_add_f32_e32 v114, 0x3727c5ac, v114
	v_mul_f32_e32 v148, 0x4f800000, v114
	v_cmp_gt_f32_e64 s[10:11], s89, v114
	v_pk_add_f32 v[18:19], v[18:19], v[112:113] op_sel_hi:[1,0] neg_lo:[0,1] neg_hi:[0,1]
	v_pk_add_f32 v[20:21], v[20:21], v[112:113] op_sel_hi:[1,0] neg_lo:[0,1] neg_hi:[0,1]
	v_cndmask_b32_e64 v114, v114, v148, s[10:11]
	v_sqrt_f32_e32 v148, v114
	v_pk_add_f32 v[14:15], v[14:15], v[112:113] op_sel_hi:[1,0] neg_lo:[0,1] neg_hi:[0,1]
	v_pk_add_f32 v[16:17], v[16:17], v[112:113] op_sel_hi:[1,0] neg_lo:[0,1] neg_hi:[0,1]
	v_pk_add_f32 v[10:11], v[10:11], v[112:113] op_sel_hi:[1,0] neg_lo:[0,1] neg_hi:[0,1]
	v_add_u32_e32 v149, -1, v148
	v_fma_f32 v158, -v149, v148, v114
	v_cmp_ge_f32_e64 s[12:13], 0, v158
	v_add_u32_e32 v158, 1, v148
	v_pk_add_f32 v[12:13], v[12:13], v[112:113] op_sel_hi:[1,0] neg_lo:[0,1] neg_hi:[0,1]
	v_cndmask_b32_e64 v149, v148, v149, s[12:13]
	v_fma_f32 v148, -v158, v148, v114
	v_cmp_lt_f32_e64 s[12:13], 0, v148
	v_pk_add_f32 v[6:7], v[6:7], v[94:95] op_sel_hi:[1,0] neg_lo:[0,1] neg_hi:[0,1]
	v_pk_add_f32 v[8:9], v[8:9], v[94:95] op_sel_hi:[1,0] neg_lo:[0,1] neg_hi:[0,1]
	v_cndmask_b32_e64 v148, v149, v158, s[12:13]
	v_mul_f32_e32 v149, 0x37800000, v148
	v_cndmask_b32_e64 v148, v148, v149, s[10:11]
	v_cmp_class_f32_e64 s[10:11], v114, v216
	v_pk_add_f32 v[2:3], v[2:3], v[112:113] op_sel_hi:[1,0] neg_lo:[0,1] neg_hi:[0,1]
	v_pk_add_f32 v[4:5], v[4:5], v[112:113] op_sel_hi:[1,0] neg_lo:[0,1] neg_hi:[0,1]
	v_cndmask_b32_e64 v148, v148, v114, s[10:11]
	v_div_scale_f32 v149, s[10:11], v148, v148, 1.0
	v_rcp_f32_e32 v158, v149
	v_div_fmas_f32 v114, v147, v167, v168
	v_div_fixup_f32 v114, v114, v116, 1.0
	v_pk_mul_f32 v[46:47], v[46:47], v[114:115] op_sel_hi:[1,0]
	v_fma_f32 v116, -v149, v158, 1.0
	v_fmac_f32_e32 v158, v116, v158
	v_div_scale_f32 v116, vcc, 1.0, v148, 1.0
	v_mul_f32_e32 v147, v116, v158
	v_fma_f32 v159, -v149, v147, v116
	v_fmac_f32_e32 v147, v159, v158
	v_fma_f32 v116, -v149, v147, v116
	v_div_fmas_f32 v116, v116, v158, v147
	v_div_fixup_f32 v116, v116, v148, 1.0
	v_lshrrev_b32_e32 v148, 3, v146
	v_bitop3_b32 v148, v148, v223, 15 bitop3:0x78
	v_lshlrev_b32_e32 v149, 4, v148
	v_lshrrev_b32_e32 v148, 1, v223
	s_waitcnt vmcnt(2)
	v_pk_fma_f32 v[82:83], v[82:83], v[238:239], v[242:243]
	v_pk_fma_f32 v[84:85], v[84:85], v[240:241], v[244:245]
	v_cvt_pk_bf16_f32 v82, v82, v83
	v_cvt_pk_bf16_f32 v83, v84, v85
	v_pk_add_f32 v[84:85], v[106:107], v[96:97] op_sel_hi:[1,0] neg_lo:[0,1] neg_hi:[0,1]
	v_pk_add_f32 v[106:107], v[108:109], v[96:97] op_sel_hi:[1,0] neg_lo:[0,1] neg_hi:[0,1]
	v_pk_mul_f32 v[84:85], v[84:85], v[110:111] op_sel_hi:[1,0]
	v_pk_mul_f32 v[106:107], v[106:107], v[110:111] op_sel_hi:[1,0]
	v_lshl_add_u32 v147, v117, 11, 0
	v_and_b32_e32 v148, 8, v148
	v_pk_fma_f32 v[84:85], v[84:85], v[238:239], v[242:243]
	v_pk_fma_f32 v[106:107], v[106:107], v[240:241], v[244:245]
	v_add3_u32 v149, v147, v149, v148
	v_cvt_pk_bf16_f32 v84, v84, v85
	v_cvt_pk_bf16_f32 v85, v106, v107
	ds_write2st64_b64 v149, v[82:83], v[84:85] offset1:64
	v_pk_add_f32 v[82:83], v[130:131], v[104:105] op_sel_hi:[1,0] neg_lo:[0,1] neg_hi:[0,1]
	v_pk_add_f32 v[84:85], v[132:133], v[104:105] op_sel_hi:[1,0] neg_lo:[0,1] neg_hi:[0,1]
	v_pk_mul_f32 v[82:83], v[82:83], v[114:115] op_sel_hi:[1,0]
	v_pk_mul_f32 v[84:85], v[84:85], v[114:115] op_sel_hi:[1,0]
	v_pk_fma_f32 v[82:83], v[82:83], v[238:239], v[242:243]
	v_pk_fma_f32 v[84:85], v[84:85], v[240:241], v[244:245]
	v_cvt_pk_bf16_f32 v82, v82, v83
	v_cvt_pk_bf16_f32 v83, v84, v85
	v_add_u32_e32 v84, 0x10000, v149
	ds_write_b64 v84, v[82:83]
	v_pk_add_f32 v[82:83], v[142:143], v[112:113] op_sel_hi:[1,0] neg_lo:[0,1] neg_hi:[0,1]
	v_pk_add_f32 v[84:85], v[144:145], v[112:113] op_sel_hi:[1,0] neg_lo:[0,1] neg_hi:[0,1]
	v_pk_mul_f32 v[82:83], v[82:83], v[116:117] op_sel_hi:[1,0]
	v_pk_mul_f32 v[84:85], v[84:85], v[116:117] op_sel_hi:[1,0]
	v_pk_fma_f32 v[82:83], v[238:239], v[82:83], v[242:243]
	v_pk_fma_f32 v[84:85], v[240:241], v[84:85], v[244:245]
	v_lshlrev_b32_e32 v238, 2, v146
	v_lshlrev_b32_e32 v242, 2, v146
	global_load_dwordx4 v[238:241], v238, s[8:9] offset:128
	global_load_dwordx4 v[242:245], v242, s[20:21] offset:128
	v_or_b32_e32 v130, 16, v146
	v_cvt_pk_bf16_f32 v82, v82, v83
	v_cvt_pk_bf16_f32 v83, v84, v85
	v_add_u32_e32 v84, 0x18000, v149
	v_ashrrev_i32_e32 v131, 31, v130
	ds_write_b64 v84, v[82:83]
	v_lshlrev_b64 v[82:83], 2, v[130:131]
	v_lshl_add_u64 v[84:85], s[8:9], 0, v[82:83]
	v_lshl_add_u64 v[106:107], s[20:21], 0, v[82:83]
	s_nop 0
	v_lshrrev_b32_e32 v130, 3, v130
	v_bitop3_b32 v130, v130, v223, 15 bitop3:0x78
	v_lshlrev_b32_e32 v130, 4, v130
	v_add3_u32 v130, v147, v130, v148
	v_pk_mul_f32 v[48:49], v[48:49], v[114:115] op_sel_hi:[1,0]
	v_pk_mul_f32 v[18:19], v[18:19], v[116:117] op_sel_hi:[1,0]
	v_pk_mul_f32 v[20:21], v[20:21], v[116:117] op_sel_hi:[1,0]
	v_pk_mul_f32 v[14:15], v[14:15], v[116:117] op_sel_hi:[1,0]
	v_pk_mul_f32 v[16:17], v[16:17], v[116:117] op_sel_hi:[1,0]
	v_pk_mul_f32 v[34:35], v[34:35], v[114:115] op_sel_hi:[1,0]
	v_pk_mul_f32 v[36:37], v[36:37], v[114:115] op_sel_hi:[1,0]
	v_pk_mul_f32 v[10:11], v[10:11], v[116:117] op_sel_hi:[1,0]
	v_pk_mul_f32 v[12:13], v[12:13], v[116:117] op_sel_hi:[1,0]
	v_pk_mul_f32 v[6:7], v[6:7], v[102:103] op_sel_hi:[1,0]
	v_pk_mul_f32 v[8:9], v[8:9], v[102:103] op_sel_hi:[1,0]
	v_pk_mul_f32 v[2:3], v[2:3], v[116:117] op_sel_hi:[1,0]
	v_pk_mul_f32 v[4:5], v[4:5], v[116:117] op_sel_hi:[1,0]
	s_add_u32 s10, s18, s14
	s_addc_u32 s11, s19, s15
	s_mov_b32 s69, s3
	s_mov_b32 s71, s3
	s_mov_b32 s47, s3
	s_mov_b32 s55, s3
	s_mov_b32 s12, 3
	s_waitcnt vmcnt(2)
	v_pk_fma_f32 v[70:71], v[70:71], v[246:247], v[250:251]
	v_pk_fma_f32 v[72:73], v[72:73], v[248:249], v[252:253]
	v_cvt_pk_bf16_f32 v70, v70, v71
	v_cvt_pk_bf16_f32 v71, v72, v73
	v_pk_add_f32 v[72:73], v[90:91], v[96:97] op_sel_hi:[1,0] neg_lo:[0,1] neg_hi:[0,1]
	v_pk_add_f32 v[90:91], v[92:93], v[96:97] op_sel_hi:[1,0] neg_lo:[0,1] neg_hi:[0,1]
	v_pk_mul_f32 v[72:73], v[72:73], v[110:111] op_sel_hi:[1,0]
	v_pk_mul_f32 v[90:91], v[90:91], v[110:111] op_sel_hi:[1,0]
	v_pk_fma_f32 v[72:73], v[72:73], v[246:247], v[250:251]
	v_pk_fma_f32 v[90:91], v[90:91], v[248:249], v[252:253]
	v_cvt_pk_bf16_f32 v72, v72, v73
	v_cvt_pk_bf16_f32 v73, v90, v91
	ds_write2st64_b64 v130, v[70:71], v[72:73] offset1:64
	v_pk_add_f32 v[70:71], v[122:123], v[104:105] op_sel_hi:[1,0] neg_lo:[0,1] neg_hi:[0,1]
	v_pk_add_f32 v[72:73], v[124:125], v[104:105] op_sel_hi:[1,0] neg_lo:[0,1] neg_hi:[0,1]
	v_pk_mul_f32 v[70:71], v[70:71], v[114:115] op_sel_hi:[1,0]
	v_pk_mul_f32 v[72:73], v[72:73], v[114:115] op_sel_hi:[1,0]
	v_pk_fma_f32 v[70:71], v[70:71], v[246:247], v[250:251]
	v_pk_fma_f32 v[72:73], v[72:73], v[248:249], v[252:253]
	v_cvt_pk_bf16_f32 v70, v70, v71
	v_cvt_pk_bf16_f32 v71, v72, v73
	v_add_u32_e32 v72, 0x10000, v130
	ds_write_b64 v72, v[70:71]
	v_pk_add_f32 v[70:71], v[138:139], v[112:113] op_sel_hi:[1,0] neg_lo:[0,1] neg_hi:[0,1]
	v_pk_add_f32 v[72:73], v[140:141], v[112:113] op_sel_hi:[1,0] neg_lo:[0,1] neg_hi:[0,1]
	v_pk_mul_f32 v[70:71], v[70:71], v[116:117] op_sel_hi:[1,0]
	v_pk_mul_f32 v[72:73], v[72:73], v[116:117] op_sel_hi:[1,0]
	v_pk_fma_f32 v[70:71], v[70:71], v[246:247], v[250:251]
	v_pk_fma_f32 v[72:73], v[72:73], v[248:249], v[252:253]
	v_lshlrev_b32_e32 v246, 2, v146
	v_lshlrev_b32_e32 v250, 2, v146
	global_load_dwordx4 v[246:249], v246, s[8:9] offset:192
	global_load_dwordx4 v[250:253], v250, s[20:21] offset:192
	v_or_b32_e32 v90, 32, v146
	v_cvt_pk_bf16_f32 v70, v70, v71
	v_cvt_pk_bf16_f32 v71, v72, v73
	v_add_u32_e32 v72, 0x18000, v130
	v_ashrrev_i32_e32 v91, 31, v90
	ds_write_b64 v72, v[70:71]
	v_lshlrev_b64 v[70:71], 2, v[90:91]
	v_lshl_add_u64 v[72:73], s[8:9], 0, v[70:71]
	v_lshl_add_u64 v[82:83], s[20:21], 0, v[70:71]
	s_nop 0
	v_lshrrev_b32_e32 v90, 3, v90
	v_bitop3_b32 v90, v90, v223, 15 bitop3:0x78
	v_lshlrev_b32_e32 v90, 4, v90
	v_add3_u32 v90, v147, v90, v148
	s_waitcnt vmcnt(2)
	v_pk_fma_f32 v[62:63], v[62:63], v[238:239], v[242:243]
	v_pk_fma_f32 v[64:65], v[64:65], v[240:241], v[244:245]
	v_cvt_pk_bf16_f32 v62, v62, v63
	v_cvt_pk_bf16_f32 v63, v64, v65
	v_pk_add_f32 v[64:65], v[86:87], v[96:97] op_sel_hi:[1,0] neg_lo:[0,1] neg_hi:[0,1]
	v_pk_add_f32 v[86:87], v[88:89], v[96:97] op_sel_hi:[1,0] neg_lo:[0,1] neg_hi:[0,1]
	v_pk_mul_f32 v[64:65], v[64:65], v[110:111] op_sel_hi:[1,0]
	v_pk_mul_f32 v[86:87], v[86:87], v[110:111] op_sel_hi:[1,0]
	v_pk_fma_f32 v[64:65], v[64:65], v[238:239], v[242:243]
	v_pk_fma_f32 v[86:87], v[86:87], v[240:241], v[244:245]
	v_cvt_pk_bf16_f32 v64, v64, v65
	v_cvt_pk_bf16_f32 v65, v86, v87
	ds_write2st64_b64 v90, v[62:63], v[64:65] offset1:64
	v_pk_add_f32 v[62:63], v[118:119], v[104:105] op_sel_hi:[1,0] neg_lo:[0,1] neg_hi:[0,1]
	v_pk_add_f32 v[64:65], v[120:121], v[104:105] op_sel_hi:[1,0] neg_lo:[0,1] neg_hi:[0,1]
	v_pk_mul_f32 v[62:63], v[62:63], v[114:115] op_sel_hi:[1,0]
	v_pk_mul_f32 v[64:65], v[64:65], v[114:115] op_sel_hi:[1,0]
	v_pk_fma_f32 v[62:63], v[62:63], v[238:239], v[242:243]
	v_pk_fma_f32 v[64:65], v[64:65], v[240:241], v[244:245]
	v_cvt_pk_bf16_f32 v62, v62, v63
	v_cvt_pk_bf16_f32 v63, v64, v65
	v_add_u32_e32 v64, 0x10000, v90
	ds_write_b64 v64, v[62:63]
	v_pk_add_f32 v[62:63], v[134:135], v[112:113] op_sel_hi:[1,0] neg_lo:[0,1] neg_hi:[0,1]
	v_pk_add_f32 v[64:65], v[136:137], v[112:113] op_sel_hi:[1,0] neg_lo:[0,1] neg_hi:[0,1]
	v_pk_mul_f32 v[62:63], v[62:63], v[116:117] op_sel_hi:[1,0]
	v_pk_mul_f32 v[64:65], v[64:65], v[116:117] op_sel_hi:[1,0]
	v_pk_fma_f32 v[62:63], v[62:63], v[238:239], v[242:243]
	v_pk_fma_f32 v[64:65], v[64:65], v[240:241], v[244:245]
	v_lshlrev_b32_e32 v238, 2, v146
	v_lshlrev_b32_e32 v242, 2, v146
	global_load_dwordx4 v[238:241], v238, s[8:9] offset:256
	global_load_dwordx4 v[242:245], v242, s[20:21] offset:256
	v_or_b32_e32 v82, 48, v146
	v_cvt_pk_bf16_f32 v62, v62, v63
	v_cvt_pk_bf16_f32 v63, v64, v65
	v_add_u32_e32 v64, 0x18000, v90
	v_ashrrev_i32_e32 v83, 31, v82
	ds_write_b64 v64, v[62:63]
	v_lshlrev_b64 v[62:63], 2, v[82:83]
	v_lshl_add_u64 v[64:65], s[8:9], 0, v[62:63]
	v_lshl_add_u64 v[70:71], s[20:21], 0, v[62:63]
	s_nop 0
	v_lshrrev_b32_e32 v82, 3, v82
	v_bitop3_b32 v82, v82, v223, 15 bitop3:0x78
	v_lshlrev_b32_e32 v82, 4, v82
	v_add3_u32 v82, v147, v82, v148
	v_lshrrev_b32_e32 v84, 4, v115
	s_waitcnt vmcnt(2)
	v_pk_fma_f32 v[58:59], v[58:59], v[246:247], v[250:251]
	v_pk_fma_f32 v[60:61], v[60:61], v[248:249], v[252:253]
	v_cvt_pk_bf16_f32 v58, v58, v59
	v_cvt_pk_bf16_f32 v59, v60, v61
	v_pk_add_f32 v[60:61], v[78:79], v[96:97] op_sel_hi:[1,0] neg_lo:[0,1] neg_hi:[0,1]
	v_pk_add_f32 v[78:79], v[80:81], v[96:97] op_sel_hi:[1,0] neg_lo:[0,1] neg_hi:[0,1]
	v_pk_mul_f32 v[60:61], v[60:61], v[110:111] op_sel_hi:[1,0]
	v_pk_mul_f32 v[78:79], v[78:79], v[110:111] op_sel_hi:[1,0]
	v_pk_fma_f32 v[60:61], v[60:61], v[246:247], v[250:251]
	v_pk_fma_f32 v[78:79], v[78:79], v[248:249], v[252:253]
	v_cvt_pk_bf16_f32 v60, v60, v61
	v_cvt_pk_bf16_f32 v61, v78, v79
	ds_write2st64_b64 v82, v[58:59], v[60:61] offset1:64
	v_pk_add_f32 v[58:59], v[98:99], v[104:105] op_sel_hi:[1,0] neg_lo:[0,1] neg_hi:[0,1]
	v_pk_add_f32 v[60:61], v[100:101], v[104:105] op_sel_hi:[1,0] neg_lo:[0,1] neg_hi:[0,1]
	v_pk_mul_f32 v[58:59], v[58:59], v[114:115] op_sel_hi:[1,0]
	v_pk_mul_f32 v[60:61], v[60:61], v[114:115] op_sel_hi:[1,0]
	v_pk_fma_f32 v[58:59], v[58:59], v[246:247], v[250:251]
	v_pk_fma_f32 v[60:61], v[60:61], v[248:249], v[252:253]
	v_cvt_pk_bf16_f32 v58, v58, v59
	v_cvt_pk_bf16_f32 v59, v60, v61
	v_add_u32_e32 v60, 0x10000, v82
	ds_write_b64 v60, v[58:59]
	v_pk_add_f32 v[58:59], v[126:127], v[112:113] op_sel_hi:[1,0] neg_lo:[0,1] neg_hi:[0,1]
	v_pk_add_f32 v[60:61], v[128:129], v[112:113] op_sel_hi:[1,0] neg_lo:[0,1] neg_hi:[0,1]
	v_pk_mul_f32 v[58:59], v[58:59], v[116:117] op_sel_hi:[1,0]
	v_pk_mul_f32 v[60:61], v[60:61], v[116:117] op_sel_hi:[1,0]
	v_pk_fma_f32 v[58:59], v[58:59], v[246:247], v[250:251]
	v_pk_fma_f32 v[60:61], v[60:61], v[248:249], v[252:253]
	v_lshlrev_b32_e32 v246, 2, v146
	v_lshlrev_b32_e32 v250, 2, v146
	global_load_dwordx4 v[246:249], v246, s[8:9] offset:320
	global_load_dwordx4 v[250:253], v250, s[20:21] offset:320
	v_or_b32_e32 v70, 64, v146
	v_cvt_pk_bf16_f32 v58, v58, v59
	v_cvt_pk_bf16_f32 v59, v60, v61
	v_add_u32_e32 v60, 0x18000, v82
	v_ashrrev_i32_e32 v71, 31, v70
	ds_write_b64 v60, v[58:59]
	v_lshlrev_b64 v[58:59], 2, v[70:71]
	v_lshl_add_u64 v[60:61], s[8:9], 0, v[58:59]
	v_lshl_add_u64 v[62:63], s[20:21], 0, v[58:59]
	s_nop 0
	v_lshrrev_b32_e32 v70, 3, v70
	v_bitop3_b32 v70, v70, v223, 15 bitop3:0x78
	v_lshlrev_b32_e32 v70, 4, v70
	v_add3_u32 v72, v147, v70, v148
	v_pk_add_f32 v[70:71], v[76:77], v[96:97] op_sel_hi:[1,0] neg_lo:[0,1] neg_hi:[0,1]
	s_waitcnt vmcnt(2)
	v_pk_fma_f32 v[54:55], v[54:55], v[238:239], v[242:243]
	v_pk_fma_f32 v[56:57], v[56:57], v[240:241], v[244:245]
	v_cvt_pk_bf16_f32 v54, v54, v55
	v_cvt_pk_bf16_f32 v55, v56, v57
	v_pk_add_f32 v[56:57], v[74:75], v[96:97] op_sel_hi:[1,0] neg_lo:[0,1] neg_hi:[0,1]
	v_pk_mul_f32 v[70:71], v[70:71], v[110:111] op_sel_hi:[1,0]
	v_pk_mul_f32 v[56:57], v[56:57], v[110:111] op_sel_hi:[1,0]
	v_pk_fma_f32 v[70:71], v[70:71], v[240:241], v[244:245]
	v_pk_fma_f32 v[56:57], v[56:57], v[238:239], v[242:243]
	v_pk_fma_f32 v[46:47], v[46:47], v[238:239], v[242:243]
	v_cvt_pk_bf16_f32 v56, v56, v57
	v_cvt_pk_bf16_f32 v57, v70, v71
	ds_write2st64_b64 v72, v[54:55], v[56:57] offset1:64
	v_pk_fma_f32 v[48:49], v[48:49], v[240:241], v[244:245]
	v_pk_fma_f32 v[18:19], v[18:19], v[238:239], v[242:243]
	v_pk_fma_f32 v[20:21], v[20:21], v[240:241], v[244:245]
	v_lshlrev_b32_e32 v238, 2, v146
	v_lshlrev_b32_e32 v242, 2, v146
	global_load_dwordx4 v[238:241], v238, s[8:9] offset:384
	global_load_dwordx4 v[242:245], v242, s[20:21] offset:384
	v_or_b32_e32 v54, 0x50, v146
	v_cvt_pk_bf16_f32 v46, v46, v47
	v_cvt_pk_bf16_f32 v47, v48, v49
	v_add_u32_e32 v48, 0x10000, v72
	v_cvt_pk_bf16_f32 v18, v18, v19
	v_cvt_pk_bf16_f32 v19, v20, v21
	v_add_u32_e32 v20, 0x18000, v72
	v_ashrrev_i32_e32 v55, 31, v54
	ds_write_b64 v48, v[46:47]
	ds_write_b64 v20, v[18:19]
	v_lshlrev_b64 v[18:19], 2, v[54:55]
	v_lshl_add_u64 v[20:21], s[8:9], 0, v[18:19]
	v_lshl_add_u64 v[46:47], s[20:21], 0, v[18:19]
	s_nop 0
	v_lshrrev_b32_e32 v54, 3, v54
	v_bitop3_b32 v54, v54, v223, 15 bitop3:0x78
	v_lshlrev_b32_e32 v54, 4, v54
	v_add3_u32 v56, v147, v54, v148
	v_pk_add_f32 v[54:55], v[66:67], v[96:97] op_sel_hi:[1,0] neg_lo:[0,1] neg_hi:[0,1]
	s_waitcnt vmcnt(2)
	v_pk_fma_f32 v[38:39], v[38:39], v[246:247], v[250:251]
	v_pk_fma_f32 v[40:41], v[40:41], v[248:249], v[252:253]
	v_cvt_pk_bf16_f32 v38, v38, v39
	v_cvt_pk_bf16_f32 v39, v40, v41
	v_pk_mul_f32 v[40:41], v[54:55], v[110:111] op_sel_hi:[1,0]
	v_pk_add_f32 v[54:55], v[68:69], v[96:97] op_sel_hi:[1,0] neg_lo:[0,1] neg_hi:[0,1]
	v_pk_fma_f32 v[40:41], v[40:41], v[246:247], v[250:251]
	v_pk_mul_f32 v[54:55], v[54:55], v[110:111] op_sel_hi:[1,0]
	v_cvt_pk_bf16_f32 v40, v40, v41
	v_pk_fma_f32 v[54:55], v[54:55], v[248:249], v[252:253]
	v_pk_fma_f32 v[14:15], v[14:15], v[246:247], v[250:251]
	v_cvt_pk_bf16_f32 v41, v54, v55
	ds_write2st64_b64 v56, v[38:39], v[40:41] offset1:64
	v_pk_add_f32 v[38:39], v[42:43], v[104:105] op_sel_hi:[1,0] neg_lo:[0,1] neg_hi:[0,1]
	v_pk_add_f32 v[40:41], v[44:45], v[104:105] op_sel_hi:[1,0] neg_lo:[0,1] neg_hi:[0,1]
	v_pk_mul_f32 v[38:39], v[38:39], v[114:115] op_sel_hi:[1,0]
	v_pk_mul_f32 v[40:41], v[40:41], v[114:115] op_sel_hi:[1,0]
	v_pk_fma_f32 v[38:39], v[38:39], v[246:247], v[250:251]
	v_pk_fma_f32 v[40:41], v[40:41], v[248:249], v[252:253]
	v_cvt_pk_bf16_f32 v38, v38, v39
	v_cvt_pk_bf16_f32 v39, v40, v41
	v_add_u32_e32 v40, 0x10000, v56
	ds_write_b64 v40, v[38:39]
	v_pk_fma_f32 v[16:17], v[16:17], v[248:249], v[252:253]
	v_lshlrev_b32_e32 v246, 2, v146
	v_lshlrev_b32_e32 v250, 2, v146
	global_load_dwordx4 v[246:249], v246, s[8:9] offset:448
	global_load_dwordx4 v[250:253], v250, s[20:21] offset:448
	v_or_b32_e32 v38, 0x60, v146
	v_cvt_pk_bf16_f32 v14, v14, v15
	v_cvt_pk_bf16_f32 v15, v16, v17
	v_add_u32_e32 v16, 0x18000, v56
	v_ashrrev_i32_e32 v39, 31, v38
	ds_write_b64 v16, v[14:15]
	v_lshlrev_b64 v[14:15], 2, v[38:39]
	v_lshl_add_u64 v[16:17], s[8:9], 0, v[14:15]
	v_lshl_add_u64 v[18:19], s[20:21], 0, v[14:15]
	s_nop 0
	v_or_b32_e32 v40, 0x70, v146
	v_lshrrev_b32_e32 v38, 3, v38
	v_pk_add_f32 v[44:45], v[50:51], v[96:97] op_sel_hi:[1,0] neg_lo:[0,1] neg_hi:[0,1]
	v_pk_add_f32 v[46:47], v[52:53], v[96:97] op_sel_hi:[1,0] neg_lo:[0,1] neg_hi:[0,1]
	v_ashrrev_i32_e32 v41, 31, v40
	v_bitop3_b32 v42, v38, v223, 15 bitop3:0x78
	v_pk_mul_f32 v[44:45], v[44:45], v[110:111] op_sel_hi:[1,0]
	v_pk_mul_f32 v[46:47], v[46:47], v[110:111] op_sel_hi:[1,0]
	v_lshlrev_b64 v[38:39], 2, v[40:41]
	v_lshlrev_b32_e32 v41, 4, v42
	v_add3_u32 v41, v147, v41, v148
	v_add_u32_e32 v48, 0x10000, v41
	v_add_u32_e32 v49, 0x18000, v41
	v_lshl_add_u64 v[42:43], s[8:9], 0, v[38:39]
	v_lshl_add_u64 v[38:39], s[20:21], 0, v[38:39]
	v_mov_b32_e32 v54, v223
	s_waitcnt vmcnt(2)
	v_pk_fma_f32 v[22:23], v[22:23], v[238:239], v[242:243]
	v_pk_fma_f32 v[24:25], v[24:25], v[240:241], v[244:245]
	v_pk_fma_f32 v[44:45], v[44:45], v[238:239], v[242:243]
	v_pk_fma_f32 v[46:47], v[46:47], v[240:241], v[244:245]
	v_pk_fma_f32 v[34:35], v[34:35], v[238:239], v[242:243]
	v_pk_fma_f32 v[36:37], v[36:37], v[240:241], v[244:245]
	v_pk_fma_f32 v[10:11], v[10:11], v[238:239], v[242:243]
	v_pk_fma_f32 v[12:13], v[12:13], v[240:241], v[244:245]
	v_cvt_pk_bf16_f32 v14, v22, v23
	v_cvt_pk_bf16_f32 v15, v24, v25
	v_cvt_pk_bf16_f32 v16, v44, v45
	v_cvt_pk_bf16_f32 v17, v46, v47
	v_cvt_pk_bf16_f32 v18, v34, v35
	v_cvt_pk_bf16_f32 v19, v36, v37
	v_cvt_pk_bf16_f32 v10, v10, v11
	v_cvt_pk_bf16_f32 v11, v12, v13
	ds_write2st64_b64 v41, v[14:15], v[16:17] offset1:64
	ds_write_b64 v48, v[18:19]
	ds_write_b64 v49, v[10:11]
	v_lshrrev_b32_e32 v18, 3, v40
	v_bitop3_b32 v18, v18, v223, 15 bitop3:0x78
	v_lshlrev_b32_e32 v18, 4, v18
	v_add3_u32 v34, v147, v18, v148
	v_pk_add_f32 v[18:19], v[26:27], v[96:97] op_sel_hi:[1,0] neg_lo:[0,1] neg_hi:[0,1]
	v_pk_add_f32 v[20:21], v[28:29], v[96:97] op_sel_hi:[1,0] neg_lo:[0,1] neg_hi:[0,1]
	v_pk_add_f32 v[22:23], v[30:31], v[104:105] op_sel_hi:[1,0] neg_lo:[0,1] neg_hi:[0,1]
	v_pk_add_f32 v[24:25], v[32:33], v[104:105] op_sel_hi:[1,0] neg_lo:[0,1] neg_hi:[0,1]
	v_pk_mul_f32 v[18:19], v[18:19], v[110:111] op_sel_hi:[1,0]
	v_pk_mul_f32 v[20:21], v[20:21], v[110:111] op_sel_hi:[1,0]
	v_pk_mul_f32 v[22:23], v[22:23], v[114:115] op_sel_hi:[1,0]
	v_pk_mul_f32 v[24:25], v[24:25], v[114:115] op_sel_hi:[1,0]
	v_add_u32_e32 v35, 0x10000, v34
	v_add_u32_e32 v36, 0x18000, v34
	s_waitcnt vmcnt(0)
	v_pk_fma_f32 v[6:7], v[6:7], v[246:247], v[250:251]
	v_pk_fma_f32 v[8:9], v[8:9], v[248:249], v[252:253]
	v_pk_fma_f32 v[18:19], v[18:19], v[246:247], v[250:251]
	v_pk_fma_f32 v[20:21], v[20:21], v[248:249], v[252:253]
	v_pk_fma_f32 v[22:23], v[22:23], v[246:247], v[250:251]
	v_pk_fma_f32 v[24:25], v[24:25], v[248:249], v[252:253]
	v_pk_fma_f32 v[2:3], v[2:3], v[246:247], v[250:251]
	v_pk_fma_f32 v[4:5], v[4:5], v[248:249], v[252:253]
	v_cvt_pk_bf16_f32 v6, v6, v7
	v_cvt_pk_bf16_f32 v7, v8, v9
	v_cvt_pk_bf16_f32 v8, v18, v19
	v_cvt_pk_bf16_f32 v9, v20, v21
	v_cvt_pk_bf16_f32 v10, v22, v23
	v_cvt_pk_bf16_f32 v11, v24, v25
	v_cvt_pk_bf16_f32 v2, v2, v3
	v_cvt_pk_bf16_f32 v3, v4, v5
	ds_write2st64_b64 v34, v[6:7], v[8:9] offset1:64
	ds_write_b64 v35, v[10:11]
	ds_write_b64 v36, v[2:3]
	s_waitcnt lgkmcnt(0)
	s_barrier
	s_nop 0
	v_and_b32_e32 v55, 0x7f, v54
	v_ashrrev_i32_e32 v4, 7, v54
	v_add_u32_e32 v2, 0x200, v54
	v_add_u32_e32 v3, 0x400, v54
	v_add_u32_e32 v7, 0x600, v54
	v_lshlrev_b32_e32 v210, 4, v55
	v_bitop3_b32 v9, v4, v55, 15 bitop3:0x6c
	v_ashrrev_i32_e32 v5, 31, v4
	v_ashrrev_i32_e32 v6, 7, v2
	v_ashrrev_i32_e32 v8, 7, v3
	v_ashrrev_i32_e32 v10, 7, v7
	v_lshlrev_b32_e32 v12, 11, v4
	v_lshl_add_u64 v[2:3], s[10:11], 0, v[210:211]
	v_lshlrev_b32_e32 v13, 4, v9
	v_lshlrev_b64 v[4:5], 11, v[4:5]
	v_bitop3_b32 v15, v6, v55, 15 bitop3:0x6c
	v_ashrrev_i32_e32 v7, 31, v6
	v_bitop3_b32 v17, v8, v55, 15 bitop3:0x6c
	v_ashrrev_i32_e32 v9, 31, v8
	v_bitop3_b32 v19, v10, v55, 15 bitop3:0x6c
	v_lshlrev_b32_e32 v14, 11, v6
	v_lshlrev_b32_e32 v16, 11, v8
	v_lshlrev_b32_e32 v18, 11, v10
	v_add3_u32 v12, 0, v12, v13
	v_lshl_add_u64 v[20:21], v[2:3], 0, v[4:5]
	v_lshlrev_b32_e32 v13, 4, v15
	v_lshlrev_b64 v[4:5], 11, v[6:7]
	v_lshlrev_b32_e32 v15, 4, v17
	v_lshlrev_b64 v[6:7], 11, v[8:9]
	v_lshlrev_b32_e32 v8, 4, v19
	v_ashrrev_i32_e32 v11, 31, v10
	v_add3_u32 v9, 0, v14, v13
	v_add3_u32 v13, 0, v16, v15
	v_add3_u32 v16, 0, v18, v8
	v_lshlrev_b64 v[22:23], 11, v[10:11]
	v_lshl_add_u64 v[24:25], v[2:3], 0, v[4:5]
	v_lshl_add_u64 v[26:27], v[2:3], 0, v[6:7]
	ds_read_b128 v[4:7], v12
	ds_read_b128 v[8:11], v9
	ds_read_b128 v[12:15], v13
	ds_read_b128 v[16:19], v16
	v_lshl_add_u64 v[22:23], v[2:3], 0, v[22:23]
	s_waitcnt lgkmcnt(3)
	global_store_dwordx4 v[20:21], v[4:7], off
	s_waitcnt lgkmcnt(2)
	global_store_dwordx4 v[24:25], v[8:11], off
	s_waitcnt lgkmcnt(1)
	global_store_dwordx4 v[26:27], v[12:15], off
	s_waitcnt lgkmcnt(0)
	global_store_dwordx4 v[22:23], v[16:19], off
	v_add_u32_e32 v4, 0x800, v54
	v_ashrrev_i32_e32 v8, 7, v4
	v_ashrrev_i32_e32 v9, 31, v8
	v_lshlrev_b32_e32 v4, 11, v8
	v_bitop3_b32 v5, v8, v55, 15 bitop3:0x6c
	v_lshlrev_b64 v[8:9], 11, v[8:9]
	v_lshl_add_u64 v[12:13], v[2:3], 0, v[8:9]
	v_add_u32_e32 v8, 0xa00, v54
	v_lshlrev_b32_e32 v5, 4, v5
	v_ashrrev_i32_e32 v14, 7, v8
	v_add3_u32 v4, 0, v4, v5
	v_bitop3_b32 v9, v14, v55, 15 bitop3:0x6c
	ds_read_b128 v[4:7], v4
	v_lshlrev_b32_e32 v8, 11, v14
	v_lshlrev_b32_e32 v9, 4, v9
	v_add3_u32 v8, 0, v8, v9
	ds_read_b128 v[8:11], v8
	v_ashrrev_i32_e32 v15, 31, v14
	s_waitcnt lgkmcnt(1)
	global_store_dwordx4 v[12:13], v[4:7], off
	s_lshl_b32 s10, s37, 9
	s_and_b32 s10, s10, 0xffff8000
	v_lshlrev_b64 v[4:5], 11, v[14:15]
	v_lshl_add_u64 v[4:5], v[2:3], 0, v[4:5]
	s_waitcnt lgkmcnt(0)
	global_store_dwordx4 v[4:5], v[8:11], off
	v_add_u32_e32 v4, 0xc00, v54
	s_ashr_i32 s11, s10, 31
	v_ashrrev_i32_e32 v8, 7, v4
	v_ashrrev_i32_e32 v9, 31, v8
	v_lshlrev_b32_e32 v4, 11, v8
	v_bitop3_b32 v5, v8, v55, 15 bitop3:0x6c
	v_lshlrev_b64 v[8:9], 11, v[8:9]
	v_lshl_add_u64 v[12:13], v[2:3], 0, v[8:9]
	v_add_u32_e32 v8, 0xe00, v54
	v_lshlrev_b32_e32 v5, 4, v5
	v_ashrrev_i32_e32 v14, 7, v8
	v_add3_u32 v4, 0, v4, v5
	v_bitop3_b32 v9, v14, v55, 15 bitop3:0x6c
	ds_read_b128 v[4:7], v4
	v_lshlrev_b32_e32 v8, 11, v14
	v_lshlrev_b32_e32 v9, 4, v9
	v_add3_u32 v8, 0, v8, v9
	ds_read_b128 v[8:11], v8
	v_ashrrev_i32_e32 v15, 31, v14
	s_waitcnt lgkmcnt(1)
	global_store_dwordx4 v[12:13], v[4:7], off
	s_lshl_b64 s[10:11], s[10:11], 1
	s_add_u32 s10, s83, s10
	v_lshlrev_b64 v[4:5], 11, v[14:15]
	v_lshl_add_u64 v[4:5], v[2:3], 0, v[4:5]
	s_waitcnt lgkmcnt(0)
	global_store_dwordx4 v[4:5], v[8:11], off
	v_add_u32_e32 v4, 0x1000, v54
	s_addc_u32 s11, s84, s11
	v_ashrrev_i32_e32 v8, 7, v4
	v_bitop3_b32 v5, v8, v55, 15 bitop3:0x6c
	v_lshlrev_b32_e32 v4, 11, v8
	v_lshlrev_b32_e32 v5, 4, v5
	v_ashrrev_i32_e32 v9, 31, v8
	v_add3_u32 v4, 0, v4, v5
	v_lshlrev_b64 v[8:9], 11, v[8:9]
	ds_read_b128 v[4:7], v4
	v_lshl_add_u64 v[12:13], v[2:3], 0, v[8:9]
	v_add_u32_e32 v8, 0x1200, v54
	v_ashrrev_i32_e32 v14, 7, v8
	v_bitop3_b32 v9, v14, v55, 15 bitop3:0x6c
	v_lshlrev_b32_e32 v8, 11, v14
	v_lshlrev_b32_e32 v9, 4, v9
	v_lshlrev_b32_e32 v210, 4, v115
	v_add3_u32 v8, 0, v8, v9
	v_lshl_add_u64 v[82:83], s[10:11], 0, v[210:211]
	ds_read_b128 v[8:11], v8
	s_waitcnt lgkmcnt(1)
	global_store_dwordx4 v[12:13], v[4:7], off
	v_ashrrev_i32_e32 v15, 31, v14
	s_nop 0
	v_lshl_add_u64 v[4:5], v[82:83], 0, s[68:69]
	v_add_co_u32_e32 v6, vcc, s88, v4
	s_nop 1
	v_addc_co_u32_e32 v7, vcc, 0, v5, vcc
	global_load_dwordx4 v[26:29], v[4:5], off
	global_load_dwordx4 v[22:25], v[6:7], off
	v_lshl_add_u64 v[4:5], v[82:83], 0, s[70:71]
	v_add_co_u32_e32 v6, vcc, s88, v4
	s_nop 1
	v_addc_co_u32_e32 v7, vcc, 0, v5, vcc
	global_load_dwordx4 v[30:33], v[4:5], off
	global_load_dwordx4 v[34:37], v[6:7], off
	v_lshl_add_u64 v[4:5], v[82:83], 0, s[46:47]
	v_add_co_u32_e32 v6, vcc, s88, v4
	s_nop 1
	v_addc_co_u32_e32 v7, vcc, 0, v5, vcc
	global_load_dwordx4 v[38:41], v[4:5], off
	global_load_dwordx4 v[42:45], v[6:7], off
	v_lshl_add_u64 v[4:5], v[82:83], 0, s[54:55]
	v_add_co_u32_e32 v6, vcc, s88, v4
	s_nop 1
	v_addc_co_u32_e32 v7, vcc, 0, v5, vcc
	global_load_dwordx4 v[50:53], v[4:5], off
	global_load_dwordx4 v[46:49], v[6:7], off
	v_lshlrev_b64 v[4:5], 11, v[14:15]
	v_lshl_add_u64 v[4:5], v[2:3], 0, v[4:5]
	s_waitcnt lgkmcnt(0)
	global_store_dwordx4 v[4:5], v[8:11], off
	v_add_u32_e32 v4, 0x1400, v54
	s_nop 0
	v_ashrrev_i32_e32 v8, 7, v4
	v_ashrrev_i32_e32 v9, 31, v8
	v_lshlrev_b32_e32 v4, 11, v8
	v_bitop3_b32 v5, v8, v55, 15 bitop3:0x6c
	v_lshlrev_b64 v[8:9], 11, v[8:9]
	v_lshl_add_u64 v[12:13], v[2:3], 0, v[8:9]
	v_add_u32_e32 v8, 0x1600, v54
	v_lshlrev_b32_e32 v5, 4, v5
	v_ashrrev_i32_e32 v14, 7, v8
	v_add3_u32 v4, 0, v4, v5
	v_bitop3_b32 v9, v14, v55, 15 bitop3:0x6c
	ds_read_b128 v[4:7], v4
	v_lshlrev_b32_e32 v8, 11, v14
	v_lshlrev_b32_e32 v9, 4, v9
	v_add3_u32 v8, 0, v8, v9
	ds_read_b128 v[8:11], v8
	v_ashrrev_i32_e32 v15, 31, v14
	s_waitcnt lgkmcnt(1)
	global_store_dwordx4 v[12:13], v[4:7], off
	s_nop 1
	v_lshlrev_b64 v[4:5], 11, v[14:15]
	v_lshl_add_u64 v[4:5], v[2:3], 0, v[4:5]
	s_waitcnt lgkmcnt(0)
	global_store_dwordx4 v[4:5], v[8:11], off
	v_add_u32_e32 v4, 0x1800, v54
	s_nop 0
	v_ashrrev_i32_e32 v8, 7, v4
	v_ashrrev_i32_e32 v9, 31, v8
	v_lshlrev_b32_e32 v4, 11, v8
	v_bitop3_b32 v5, v8, v55, 15 bitop3:0x6c
	v_lshlrev_b64 v[8:9], 11, v[8:9]
	v_lshl_add_u64 v[12:13], v[2:3], 0, v[8:9]
	v_add_u32_e32 v8, 0x1a00, v54
	v_lshlrev_b32_e32 v5, 4, v5
	v_ashrrev_i32_e32 v14, 7, v8
	v_add3_u32 v4, 0, v4, v5
	v_bitop3_b32 v9, v14, v55, 15 bitop3:0x6c
	ds_read_b128 v[4:7], v4
	v_lshlrev_b32_e32 v8, 11, v14
	v_lshlrev_b32_e32 v9, 4, v9
	v_add3_u32 v8, 0, v8, v9
	ds_read_b128 v[8:11], v8
	v_ashrrev_i32_e32 v15, 31, v14
	s_waitcnt lgkmcnt(1)
	global_store_dwordx4 v[12:13], v[4:7], off
	s_nop 1
	v_lshlrev_b64 v[4:5], 11, v[14:15]
	v_lshl_add_u64 v[4:5], v[2:3], 0, v[4:5]
	s_waitcnt lgkmcnt(0)
	global_store_dwordx4 v[4:5], v[8:11], off
	v_add_u32_e32 v4, 0x1c00, v54
	s_nop 0
	v_ashrrev_i32_e32 v8, 7, v4
	v_bitop3_b32 v5, v8, v55, 15 bitop3:0x6c
	v_lshlrev_b32_e32 v4, 11, v8
	v_lshlrev_b32_e32 v5, 4, v5
	v_ashrrev_i32_e32 v9, 31, v8
	v_add3_u32 v4, 0, v4, v5
	v_lshlrev_b64 v[8:9], 11, v[8:9]
	ds_read_b128 v[4:7], v4
	v_lshl_add_u64 v[12:13], v[2:3], 0, v[8:9]
	v_add_u32_e32 v8, 0x1e00, v54
	v_ashrrev_i32_e32 v14, 7, v8
	v_bitop3_b32 v9, v14, v55, 15 bitop3:0x6c
	v_lshlrev_b32_e32 v8, 11, v14
	v_lshlrev_b32_e32 v9, 4, v9
	v_add3_u32 v8, 0, v8, v9
	ds_read_b128 v[8:11], v8
	s_waitcnt lgkmcnt(1)
	global_store_dwordx4 v[12:13], v[4:7], off
	v_ashrrev_i32_e32 v15, 31, v14
	s_nop 0
	v_bitop3_b32 v4, v84, v117, s81 bitop3:0x36
	v_lshl_add_u32 v4, v4, 4, v147
	v_add_u32_e32 v5, 0x10000, v4
	ds_read_b128 v[62:65], v4
	ds_read_b128 v[66:69], v4 offset:32768
	v_add_u32_e32 v4, 0x18000, v4
	ds_read_b128 v[74:77], v5
	ds_read_b128 v[70:73], v4
	v_lshlrev_b64 v[4:5], 11, v[14:15]
	v_lshl_add_u64 v[2:3], v[2:3], 0, v[4:5]
	s_waitcnt lgkmcnt(4)
	global_store_dwordx4 v[2:3], v[8:11], off
	v_mov_b32_e32 v2, 0
	s_mov_b32 s13, s85
	v_mov_b32_e32 v3, v2
	v_mov_b32_e32 v4, v2
	v_mov_b32_e32 v5, v2
	v_mov_b32_e32 v6, v2
	v_mov_b32_e32 v7, v2
	v_mov_b32_e32 v8, v2
	v_mov_b32_e32 v9, v2
	v_mov_b32_e32 v10, v2
	v_mov_b32_e32 v11, v2
	v_mov_b32_e32 v12, v2
	v_mov_b32_e32 v13, v2
	v_mov_b32_e32 v14, v2
	v_mov_b32_e32 v15, v2
	v_mov_b32_e32 v16, v2
	v_mov_b32_e32 v17, v2
	v_mov_b32_e32 v18, v2
	v_mov_b32_e32 v19, v2
	v_mov_b32_e32 v20, v2
	v_mov_b32_e32 v21, v2
	v_mov_b32_e32 v54, v2
	v_mov_b32_e32 v55, v2
	v_mov_b32_e32 v56, v2
	v_mov_b32_e32 v57, v2
	v_mov_b32_e32 v58, v2
	v_mov_b32_e32 v59, v2
	v_mov_b32_e32 v60, v2
	v_mov_b32_e32 v61, v2
	v_mov_b32_e32 v78, v2
	v_mov_b32_e32 v79, v2
	v_mov_b32_e32 v80, v2
	v_mov_b32_e32 v81, v2
